# speedup vs baseline: 1.0688x; 1.0097x over previous
.LBB1_5:
	s_andn2_b64 vcc, exec, s[4:5]
	s_cbranch_vccnz .LBB1_41
	s_load_dwordx4 s[4:7], s[0:1], 0x0
	s_load_dwordx2 s[8:9], s[0:1], 0x40
	v_lshlrev_b32_e32 v2, 4, v0
	s_mov_b32 s29, 0
	v_mov_b32_e32 v3, 0
	s_lshl_b32 s28, s2, 4
	s_waitcnt lgkmcnt(0)
	v_lshl_add_u64 v[96:97], s[4:5], 0, v[2:3]
	s_lshl_b64 s[4:5], s[28:29], 12
	v_lshl_add_u64 v[4:5], v[96:97], 0, s[4:5]
	s_or_b32 s4, s28, 1
	s_mov_b32 s5, s29
	s_lshl_b64 s[10:11], s[4:5], 12
	s_or_b32 s20, s28, 2
	s_mov_b32 s21, s29
	v_lshl_add_u64 v[6:7], v[96:97], 0, s[10:11]
	global_load_dwordx4 v[30:33], v[4:5], off nt
	global_load_dwordx4 v[26:29], v[6:7], off nt
	s_lshl_b64 s[10:11], s[20:21], 12
	s_or_b32 s18, s28, 3
	s_mov_b32 s19, s29
	v_lshl_add_u64 v[4:5], v[96:97], 0, s[10:11]
	s_lshl_b64 s[10:11], s[18:19], 12
	global_load_dwordx4 v[22:25], v[4:5], off nt
	v_lshl_add_u64 v[4:5], v[96:97], 0, s[10:11]
	global_load_dwordx4 v[18:21], v[4:5], off nt
	s_or_b32 s16, s28, 4
	s_mov_b32 s17, s29
	s_lshl_b64 s[10:11], s[16:17], 12
	v_lshl_add_u64 v[4:5], v[96:97], 0, s[10:11]
	global_load_dwordx4 v[14:17], v[4:5], off nt
	s_or_b32 s14, s28, 5
	s_mov_b32 s15, s29
	s_lshl_b64 s[24:25], s[14:15], 12
	v_lshl_add_u64 v[42:43], s[6:7], 0, v[2:3]
	s_or_b32 s12, s28, 6
	s_mov_b32 s13, s29
	v_lshl_add_u64 v[4:5], v[96:97], 0, s[24:25]
	global_load_dwordx4 v[34:37], v2, s[6:7]
	v_lshlrev_b32_e32 v2, 3, v0
	v_add_co_u32_e32 v48, vcc, 0x1000, v42
	s_or_b32 s10, s28, 7
	s_mov_b32 s11, s29
	s_lshl_b64 s[26:27], s[12:13], 12
	global_load_dwordx4 v[10:13], v[4:5], off nt
	s_lshl_b64 s[4:5], s[4:5], 11
	v_lshl_add_u64 v[94:95], s[8:9], 0, v[2:3]
	s_mov_b64 s[6:7], vcc
	v_add_co_u32_e32 v46, vcc, 0x2000, v42
	s_lshl_b64 s[30:31], s[10:11], 12
	v_lshl_add_u64 v[38:39], v[96:97], 0, s[26:27]
	v_lshl_add_u64 v[52:53], v[94:95], 0, s[4:5]
	s_mov_b64 s[4:5], vcc
	v_add_co_u32_e32 v44, vcc, 0x3000, v42
	v_lshl_add_u64 v[40:41], v[96:97], 0, s[30:31]
	global_load_dwordx4 v[6:9], v[38:39], off nt
	global_load_dwordx4 v[2:5], v[40:41], off nt
	s_mov_b64 s[8:9], vcc
	v_add_co_u32_e32 v38, vcc, 0x4000, v42
	s_lshl_b64 s[22:23], s[28:29], 11
	s_nop 0
	v_addc_co_u32_e32 v39, vcc, 0, v43, vcc
	v_addc_co_u32_e64 v49, vcc, 0, v43, s[6:7]
	global_load_dwordx4 v[38:41], v[38:39], off
	v_lshl_add_u64 v[50:51], v[94:95], 0, s[22:23]
	global_load_dwordx4 v[54:57], v[48:49], off
	v_add_co_u32_e32 v48, vcc, 0x5000, v42
	s_lshl_b64 s[20:21], s[20:21], 11
	s_nop 0
	v_addc_co_u32_e32 v49, vcc, 0, v43, vcc
	global_load_dwordx4 v[58:61], v[48:49], off
	s_lshl_b64 s[6:7], s[18:19], 11
	s_movk_i32 s3, 0xc0
	s_waitcnt vmcnt(11)
	v_cvt_f16_f32_e32 v1, v30
	v_cvt_f16_f32_e32 v45, v33
	v_cvt_pk_f16_f32 v47, v31, v32
	s_waitcnt vmcnt(10)
	v_cvt_f16_f32_e32 v62, v26
	v_cvt_f16_f32_e32 v63, v29
	v_pack_b32_f16 v48, v1, v47
	v_alignbit_b32 v49, v45, v47, 16
	v_cvt_pk_f16_f32 v64, v27, v28
	v_pack_b32_f16 v62, v62, v64
	s_waitcnt vmcnt(8)
	v_cvt_f16_f32_e32 v1, v18
	v_cvt_f16_f32_e32 v47, v21
	v_cvt_pk_f16_f32 v45, v19, v20
	v_alignbit_b32 v63, v63, v64, 16
	global_store_dwordx2 v[50:51], v[48:49], off
	global_store_dwordx2 v[52:53], v[62:63], off
	v_pack_b32_f16 v50, v1, v45
	v_alignbit_b32 v51, v47, v45, 16
	s_waitcnt vmcnt(9)
	v_cvt_f16_f32_e32 v1, v14
	v_cvt_f16_f32_e32 v45, v17
	v_addc_co_u32_e64 v47, vcc, 0, v43, s[4:5]
	global_load_dwordx4 v[68:71], v[46:47], off
	v_add_co_u32_e32 v46, vcc, 0x6000, v42
	v_cvt_f16_f32_e32 v65, v22
	s_nop 0
	v_addc_co_u32_e32 v47, vcc, 0, v43, vcc
	global_load_dwordx4 v[86:89], v[46:47], off
	v_cvt_pk_f16_f32 v47, v15, v16
	v_pack_b32_f16 v46, v1, v47
	v_alignbit_b32 v47, v45, v47, 16
	v_addc_co_u32_e64 v45, vcc, 0, v43, s[8:9]
	global_load_dwordx4 v[98:101], v[44:45], off
	v_add_co_u32_e32 v42, vcc, 0x7000, v42
	v_cvt_f16_f32_e32 v67, v25
	s_nop 0
	v_addc_co_u32_e32 v43, vcc, 0, v43, vcc
	global_load_dwordx4 v[102:105], v[42:43], off
	v_cvt_pk_f16_f32 v66, v23, v24
	v_pack_b32_f16 v48, v65, v66
	v_alignbit_b32 v49, v67, v66, 16
	v_lshl_add_u64 v[52:53], v[94:95], 0, s[20:21]
	s_waitcnt vmcnt(11)
	v_cvt_f16_f32_e32 v1, v10
	global_store_dwordx2 v[52:53], v[48:49], off
	v_lshl_add_u64 v[48:49], v[94:95], 0, s[6:7]
	s_lshl_b64 s[4:5], s[16:17], 11
	global_store_dwordx2 v[48:49], v[50:51], off
	v_lshl_add_u64 v[48:49], v[94:95], 0, s[4:5]
	v_cvt_f16_f32_e32 v50, v13
	global_store_dwordx2 v[48:49], v[46:47], off
	v_cvt_pk_f16_f32 v47, v11, v12
	v_pack_b32_f16 v46, v1, v47
	s_waitcnt vmcnt(13)
	v_cvt_f16_f32_e32 v1, v6
	v_cvt_f16_f32_e32 v44, v9
	s_lshl_b64 s[4:5], s[14:15], 11
	v_alignbit_b32 v47, v50, v47, 16
	v_lshl_add_u64 v[42:43], v[94:95], 0, s[4:5]
	global_store_dwordx2 v[42:43], v[46:47], off
	v_cvt_pk_f16_f32 v42, v7, v8
	v_pack_b32_f16 v108, v1, v42
	v_alignbit_b32 v109, v44, v42, 16
	v_cvt_f64_f32_e32 v[52:53], v35
	s_waitcnt vmcnt(12)
	v_cvt_f64_f32_e32 v[42:43], v39
	v_cvt_f64_f32_e32 v[110:111], v31
	v_cvt_f64_f32_e32 v[48:49], v34
	v_cvt_f64_f32_e32 v[50:51], v36
	v_cvt_f64_f32_e32 v[46:47], v37
	v_cvt_f64_f32_e32 v[36:37], v38
	v_cvt_f64_f32_e32 v[106:107], v30
	v_cvt_f64_f32_e32 v[112:113], v32
	v_cvt_f64_f32_e32 v[114:115], v33
	v_mul_f64 v[30:31], v[52:53], v[110:111]
	v_mul_f64 v[32:33], v[42:43], v[110:111]
	v_cvt_f64_f32_e32 v[38:39], v40
	v_fmac_f64_e32 v[30:31], v[48:49], v[106:107]
	v_fmac_f64_e32 v[32:33], v[36:37], v[106:107]
	v_cvt_f64_f32_e32 v[34:35], v41
	v_fmac_f64_e32 v[30:31], v[50:51], v[112:113]
	v_fmac_f64_e32 v[32:33], v[38:39], v[112:113]
	v_and_b32_e32 v1, 1, v0
	v_fmac_f64_e32 v[30:31], v[46:47], v[114:115]
	v_fmac_f64_e32 v[32:33], v[34:35], v[114:115]
	v_cmp_eq_u32_e32 vcc, 0, v1
	s_waitcnt vmcnt(11)
	v_cvt_f64_f32_e32 v[74:75], v55
	s_waitcnt vmcnt(10)
	v_cvt_f64_f32_e32 v[44:45], v59
	v_cndmask_b32_e32 v1, v31, v33, vcc
	v_cndmask_b32_e32 v117, v33, v31, vcc
	v_cndmask_b32_e32 v116, v32, v30, vcc
	v_cndmask_b32_e32 v122, v30, v32, vcc
	v_cvt_f64_f32_e32 v[64:65], v54
	v_cvt_f64_f32_e32 v[66:67], v56
	v_cvt_f64_f32_e32 v[62:63], v57
	v_cvt_f64_f32_e32 v[32:33], v58
	v_mul_f64 v[54:55], v[74:75], v[110:111]
	v_mul_f64 v[56:57], v[44:45], v[110:111]
	v_cvt_f64_f32_e32 v[40:41], v60
	v_fmac_f64_e32 v[54:55], v[64:65], v[106:107]
	v_fmac_f64_e32 v[56:57], v[32:33], v[106:107]
	v_cvt_f64_f32_e32 v[30:31], v61
	v_fmac_f64_e32 v[54:55], v[66:67], v[112:113]
	v_fmac_f64_e32 v[56:57], v[40:41], v[112:113]
	v_fmac_f64_e32 v[54:55], v[62:63], v[114:115]
	v_fmac_f64_e32 v[56:57], v[30:31], v[114:115]
	s_waitcnt vmcnt(7)
	v_cvt_f64_f32_e32 v[84:85], v69
	v_cndmask_b32_e32 v119, v57, v55, vcc
	s_waitcnt vmcnt(6)
	v_cvt_f64_f32_e32 v[60:61], v87
	v_cndmask_b32_e32 v118, v56, v54, vcc
	v_cndmask_b32_e32 v123, v55, v57, vcc
	v_cndmask_b32_e32 v124, v54, v56, vcc
	v_cvt_f64_f32_e32 v[80:81], v68
	v_cvt_f64_f32_e32 v[82:83], v70
	s_waitcnt vmcnt(5)
	v_cvt_f64_f32_e32 v[90:91], v100
	v_mbcnt_lo_u32_b32 v100, -1, 0
	v_mbcnt_hi_u32_b32 v100, -1, v100
	v_cvt_f64_f32_e32 v[78:79], v71
	v_cvt_f64_f32_e32 v[56:57], v86
	v_mul_f64 v[68:69], v[84:85], v[110:111]
	v_mul_f64 v[70:71], v[60:61], v[110:111]
	v_cvt_f64_f32_e32 v[86:87], v101
	v_and_b32_e32 v101, 64, v100
	v_cvt_f64_f32_e32 v[58:59], v88
	v_fmac_f64_e32 v[68:69], v[80:81], v[106:107]
	v_fmac_f64_e32 v[70:71], v[56:57], v[106:107]
	v_add_u32_e32 v127, 64, v101
	v_xor_b32_e32 v101, 1, v100
	v_cvt_f64_f32_e32 v[54:55], v89
	v_fmac_f64_e32 v[68:69], v[82:83], v[112:113]
	v_fmac_f64_e32 v[70:71], v[58:59], v[112:113]
	v_cmp_lt_i32_e64 s[4:5], v101, v127
	v_fmac_f64_e32 v[68:69], v[78:79], v[114:115]
	v_fmac_f64_e32 v[70:71], v[54:55], v[114:115]
	v_cndmask_b32_e64 v101, v100, v101, s[4:5]
	v_cndmask_b32_e32 v125, v69, v71, vcc
	v_cndmask_b32_e32 v126, v68, v70, vcc
	v_cvt_f64_f32_e32 v[92:93], v99
	s_waitcnt vmcnt(4)
	v_cvt_f64_f32_e32 v[76:77], v103
	v_lshlrev_b32_e32 v101, 2, v101
	v_cndmask_b32_e32 v121, v71, v69, vcc
	v_cndmask_b32_e32 v120, v70, v68, vcc
	v_cvt_f64_f32_e32 v[88:89], v98
	v_cvt_f64_f32_e32 v[70:71], v102
	v_mul_f64 v[98:99], v[92:93], v[110:111]
	v_mul_f64 v[102:103], v[76:77], v[110:111]
	ds_bpermute_b32 v110, v101, v126
	ds_bpermute_b32 v111, v101, v125
	v_cvt_f64_f32_e32 v[72:73], v104
	v_fmac_f64_e32 v[98:99], v[88:89], v[106:107]
	v_fmac_f64_e32 v[102:103], v[70:71], v[106:107]
	v_cvt_f64_f32_e32 v[68:69], v105
	v_fmac_f64_e32 v[98:99], v[90:91], v[112:113]
	v_fmac_f64_e32 v[102:103], v[72:73], v[112:113]
	ds_bpermute_b32 v106, v101, v122
	ds_bpermute_b32 v107, v101, v1
	v_fmac_f64_e32 v[98:99], v[86:87], v[114:115]
	v_fmac_f64_e32 v[102:103], v[68:69], v[114:115]
	v_cndmask_b32_e32 v1, v99, v103, vcc
	v_cndmask_b32_e32 v112, v98, v102, vcc
	v_cndmask_b32_e32 v105, v103, v99, vcc
	v_cndmask_b32_e32 v104, v102, v98, vcc
	s_waitcnt lgkmcnt(2)
	v_add_f64 v[102:103], v[120:121], v[110:111]
	ds_bpermute_b32 v110, v101, v112
	ds_bpermute_b32 v111, v101, v1
	s_waitcnt lgkmcnt(2)
	v_add_f64 v[98:99], v[116:117], v[106:107]
	ds_bpermute_b32 v106, v101, v124
	ds_bpermute_b32 v107, v101, v123
	v_and_b32_e32 v113, 2, v0
	s_waitcnt lgkmcnt(2)
	v_add_f64 v[110:111], v[104:105], v[110:111]
	v_xor_b32_e32 v104, 2, v100
	v_cmp_lt_i32_e64 s[4:5], v104, v127
	v_cmp_eq_u32_e64 s[8:9], 0, v113
	s_waitcnt lgkmcnt(0)
	v_add_f64 v[106:107], v[118:119], v[106:107]
	v_cndmask_b32_e64 v104, v100, v104, s[4:5]
	v_cndmask_b32_e64 v113, v103, v99, s[8:9]
	v_cndmask_b32_e64 v1, v99, v103, s[8:9]
	v_cndmask_b32_e64 v99, v98, v102, s[8:9]
	v_cndmask_b32_e64 v103, v107, v111, s[8:9]
	v_cndmask_b32_e64 v105, v106, v110, s[8:9]
	v_lshlrev_b32_e32 v104, 2, v104
	ds_bpermute_b32 v114, v104, v99
	ds_bpermute_b32 v115, v104, v1
	ds_bpermute_b32 v116, v104, v105
	ds_bpermute_b32 v117, v104, v103
	v_cndmask_b32_e64 v112, v102, v98, s[8:9]
	v_cndmask_b32_e64 v99, v111, v107, s[8:9]
	v_cndmask_b32_e64 v98, v110, v106, s[8:9]
	v_and_b32_e32 v1, 4, v0
	s_waitcnt lgkmcnt(2)
	v_add_f64 v[102:103], v[112:113], v[114:115]
	s_waitcnt lgkmcnt(0)
	v_add_f64 v[98:99], v[98:99], v[116:117]
	v_cmp_eq_u32_e64 s[4:5], 0, v1
	s_nop 1
	v_cndmask_b32_e64 v107, v99, v103, s[4:5]
	v_cndmask_b32_e64 v1, v103, v99, s[4:5]
	v_xor_b32_e32 v103, 4, v100
	v_cmp_lt_i32_e64 s[6:7], v103, v127
	v_cndmask_b32_e64 v99, v102, v98, s[4:5]
	v_cndmask_b32_e64 v106, v98, v102, s[4:5]
	v_cndmask_b32_e64 v103, v100, v103, s[6:7]
	v_lshlrev_b32_e32 v105, 2, v103
	ds_bpermute_b32 v110, v105, v99
	ds_bpermute_b32 v111, v105, v1
	s_lshl_b64 s[6:7], s[12:13], 11
	v_xor_b32_e32 v102, 8, v100
	v_lshl_add_u64 v[112:113], v[94:95], 0, s[6:7]
	v_cmp_lt_i32_e64 s[6:7], v102, v127
	v_cvt_f16_f32_e32 v1, v2
	s_waitcnt lgkmcnt(0)
	v_add_f64 v[98:99], v[106:107], v[110:111]
	v_cndmask_b32_e64 v102, v100, v102, s[6:7]
	v_lshlrev_b32_e32 v106, 2, v102
	ds_bpermute_b32 v102, v106, v98
	ds_bpermute_b32 v103, v106, v99
	v_cvt_pk_f16_f32 v110, v3, v4
	global_store_dwordx2 v[112:113], v[108:109], off
	v_pack_b32_f16 v108, v1, v110
	v_xor_b32_e32 v1, 16, v100
	v_cmp_lt_i32_e64 s[6:7], v1, v127
	v_cvt_f16_f32_e32 v109, v5
	s_waitcnt lgkmcnt(0)
	v_add_f64 v[98:99], v[98:99], v[102:103]
	v_cndmask_b32_e64 v1, v100, v1, s[6:7]
	v_lshlrev_b32_e32 v107, 2, v1
	ds_bpermute_b32 v102, v107, v98
	ds_bpermute_b32 v103, v107, v99
	s_lshl_b64 s[6:7], s[10:11], 11
	v_xor_b32_e32 v1, 32, v100
	v_alignbit_b32 v109, v109, v110, 16
	v_lshl_add_u64 v[110:111], v[94:95], 0, s[6:7]
	v_cmp_lt_i32_e64 s[6:7], v1, v127
	global_store_dwordx2 v[110:111], v[108:109], off
	s_waitcnt lgkmcnt(0)
	v_add_f64 v[98:99], v[98:99], v[102:103]
	v_cndmask_b32_e64 v1, v100, v1, s[6:7]
	v_lshlrev_b32_e32 v109, 2, v1
	ds_bpermute_b32 v102, v109, v98
	ds_bpermute_b32 v103, v109, v99
	v_bfrev_b32_e32 v1, v0
	v_lshrrev_b32_e32 v1, 26, v1
	v_and_b32_e32 v100, 56, v0
	v_and_b32_e32 v1, 56, v1
	v_cmp_eq_u32_e64 s[6:7], 0, v100
	v_and_or_b32 v108, v0, s3, v1
	v_mov_b32_e32 v100, v27
	v_mov_b32_e32 v27, v28
	v_mov_b32_e32 v28, v23
	v_mov_b32_e32 v23, v24
	v_mov_b32_e32 v24, v19
	v_mov_b32_e32 v19, v20
	v_mov_b32_e32 v20, v15
	v_mov_b32_e32 v15, v16
	v_mov_b32_e32 v16, v11
	v_mov_b32_e32 v11, v12
	v_mov_b32_e32 v12, v7
	v_mov_b32_e32 v7, v8
	v_mov_b32_e32 v8, v3
	v_mov_b32_e32 v1, v4
	s_and_saveexec_b64 s[10:11], s[6:7]
	s_cbranch_execz .LBB1_8
	s_waitcnt lgkmcnt(0)
	v_add_f64 v[98:99], v[98:99], v[102:103]
	ds_write_b64 v108, v[98:99]
